# router top-k: the 32 serial per-expert bias loads replaced by one preload + v_readlane (bit-identical arithmetic)
# speedup vs baseline: 1.0058x; 1.0016x over previous
.LBB0_867:
	s_andn2_saveexec_b64 s[6:7], s[6:7]
	s_cbranch_execz .LBB0_897
	s_movk_i32 s1, 0x84
	v_lshlrev_b32_e32 v30, 2, v16
	global_load_dword v30, v30, s[64:65]
	v_mul_lo_u32 v0, v16, s1
	s_mov_b32 s9, 0
	v_add_u32_e32 v7, 0, v0
	v_mov_b32_e32 v8, 0
	v_mov_b32_e32 v4, 0xff61b1e6
	v_mov_b32_e32 v5, 0xff61b1e6
	v_mov_b32_e32 v6, 0xff61b1e6
	v_mov_b32_e32 v10, 0xff61b1e6
	v_mov_b32_e32 v0, 0
	v_mov_b32_e32 v3, 0
	v_mov_b32_e32 v1, 0
	v_mov_b32_e32 v2, 0
	s_mov_b32 s8, s9
	s_waitcnt vmcnt(0)
	s_branch .LBB0_872

.LBB0_872:
	s_lshl_b64 s[2:3], s[8:9], 2
	s_add_u32 s10, s64, s2
	s_addc_u32 s11, s65, s3
	v_readlane_b32 s3, v30, s8
	v_lshl_add_u32 v9, s8, 2, v7
	ds_read_b32 v12, v9
	ds_read_b32 v13, v9 offset:4224
	ds_read_b32 v14, v9 offset:8448
	ds_read_b32 v15, v9 offset:12672
	ds_read_b32 v17, v9 offset:16896
	ds_read_b32 v18, v9 offset:21120
	ds_read_b32 v19, v9 offset:25344
	ds_read_b32 v20, v9 offset:29568
	s_waitcnt lgkmcnt(7)
	v_add_f32_e32 v11, s3, v12
	s_waitcnt lgkmcnt(6)
	v_add_f32_e32 v11, v11, v13
	s_waitcnt lgkmcnt(5)
	v_add_f32_e32 v11, v11, v14
	s_waitcnt lgkmcnt(4)
	v_add_f32_e32 v11, v11, v15
	s_waitcnt lgkmcnt(3)
	v_add_f32_e32 v11, v11, v17
	s_waitcnt lgkmcnt(2)
	v_add_f32_e32 v11, v11, v18
	s_waitcnt lgkmcnt(1)
	v_add_f32_e32 v11, v11, v19
	s_waitcnt lgkmcnt(0)
	v_add_f32_e32 v11, v11, v20
	v_cmp_gt_f32_e32 vcc, v11, v10
	s_and_saveexec_b64 s[12:13], vcc
	s_cbranch_execz .LBB0_878
	v_cmp_gt_f32_e32 vcc, v11, v6
	v_mov_b32_e32 v3, s8
	s_and_saveexec_b64 s[14:15], vcc
	s_cbranch_execz .LBB0_877
	v_cmp_gt_f32_e32 vcc, v11, v5
	v_mov_b32_e32 v10, s8
	s_and_saveexec_b64 s[16:17], vcc
	s_cbranch_execz .LBB0_876
	v_mov_b32_e32 v3, s8
	v_cmp_gt_f32_e32 vcc, v11, v4
	v_mov_b32_e32 v10, v1
	s_nop 0
	v_cndmask_b32_e32 v12, v3, v0, vcc
	v_cndmask_b32_e32 v0, v0, v3, vcc
	v_cndmask_b32_e32 v3, v11, v4, vcc
	v_cndmask_b32_e32 v4, v4, v11, vcc
	v_mov_b32_e32 v1, v12
	v_mov_b32_e32 v11, v5
	v_mov_b32_e32 v5, v3

.LBB0_878:
	s_or_b64 exec, exec, s[12:13]
	s_add_i32 s2, s8, 1
	v_readlane_b32 s3, v30, s2
	ds_read_b32 v12, v9 offset:4
	ds_read_b32 v13, v9 offset:4228
	ds_read_b32 v14, v9 offset:8452
	ds_read_b32 v15, v9 offset:12676
	ds_read_b32 v17, v9 offset:16900
	ds_read_b32 v18, v9 offset:21124
	ds_read_b32 v19, v9 offset:25348
	ds_read_b32 v20, v9 offset:29572
	s_waitcnt lgkmcnt(7)
	v_add_f32_e32 v11, s3, v12
	s_waitcnt lgkmcnt(6)
	v_add_f32_e32 v11, v11, v13
	s_waitcnt lgkmcnt(5)
	v_add_f32_e32 v11, v11, v14
	s_waitcnt lgkmcnt(4)
	v_add_f32_e32 v11, v11, v15
	s_waitcnt lgkmcnt(3)
	v_add_f32_e32 v11, v11, v17
	s_waitcnt lgkmcnt(2)
	v_add_f32_e32 v11, v11, v18
	s_waitcnt lgkmcnt(1)
	v_add_f32_e32 v11, v11, v19
	s_waitcnt lgkmcnt(0)
	v_add_f32_e32 v11, v11, v20
	v_cmp_gt_f32_e32 vcc, v11, v10
	s_and_saveexec_b64 s[12:13], vcc
	s_cbranch_execz .LBB0_884
	s_add_i32 s1, s8, 1
	v_cmp_gt_f32_e32 vcc, v11, v6
	v_mov_b32_e32 v3, s1
	s_and_saveexec_b64 s[14:15], vcc
	s_cbranch_execz .LBB0_883
	v_cmp_gt_f32_e32 vcc, v11, v5
	v_mov_b32_e32 v10, s1
	s_and_saveexec_b64 s[16:17], vcc
	s_cbranch_execz .LBB0_882
	v_mov_b32_e32 v3, s1
	v_cmp_gt_f32_e32 vcc, v11, v4
	v_mov_b32_e32 v10, v1
	s_nop 0
	v_cndmask_b32_e32 v12, v3, v0, vcc
	v_cndmask_b32_e32 v0, v0, v3, vcc
	v_cndmask_b32_e32 v3, v11, v4, vcc
	v_cndmask_b32_e32 v4, v4, v11, vcc
	v_mov_b32_e32 v1, v12
	v_mov_b32_e32 v11, v5
	v_mov_b32_e32 v5, v3

.LBB0_884:
	s_or_b64 exec, exec, s[12:13]
	s_add_i32 s2, s8, 2
	v_readlane_b32 s3, v30, s2
	ds_read_b32 v12, v9 offset:8
	ds_read_b32 v13, v9 offset:4232
	ds_read_b32 v14, v9 offset:8456
	ds_read_b32 v15, v9 offset:12680
	ds_read_b32 v17, v9 offset:16904
	ds_read_b32 v18, v9 offset:21128
	ds_read_b32 v19, v9 offset:25352
	ds_read_b32 v20, v9 offset:29576
	s_waitcnt lgkmcnt(7)
	v_add_f32_e32 v11, s3, v12
	s_waitcnt lgkmcnt(6)
	v_add_f32_e32 v11, v11, v13
	s_waitcnt lgkmcnt(5)
	v_add_f32_e32 v11, v11, v14
	s_waitcnt lgkmcnt(4)
	v_add_f32_e32 v11, v11, v15
	s_waitcnt lgkmcnt(3)
	v_add_f32_e32 v11, v11, v17
	s_waitcnt lgkmcnt(2)
	v_add_f32_e32 v11, v11, v18
	s_waitcnt lgkmcnt(1)
	v_add_f32_e32 v11, v11, v19
	s_waitcnt lgkmcnt(0)
	v_add_f32_e32 v11, v11, v20
	v_cmp_gt_f32_e32 vcc, v11, v10
	s_and_saveexec_b64 s[12:13], vcc
	s_cbranch_execz .LBB0_890
	s_add_i32 s1, s8, 2
	v_cmp_gt_f32_e32 vcc, v11, v6
	v_mov_b32_e32 v3, s1
	s_and_saveexec_b64 s[14:15], vcc
	s_cbranch_execz .LBB0_889
	v_cmp_gt_f32_e32 vcc, v11, v5
	v_mov_b32_e32 v10, s1
	s_and_saveexec_b64 s[16:17], vcc
	s_cbranch_execz .LBB0_888
	v_mov_b32_e32 v3, s1
	v_cmp_gt_f32_e32 vcc, v11, v4
	v_mov_b32_e32 v10, v1
	s_nop 0
	v_cndmask_b32_e32 v12, v3, v0, vcc
	v_cndmask_b32_e32 v0, v0, v3, vcc
	v_cndmask_b32_e32 v3, v11, v4, vcc
	v_cndmask_b32_e32 v4, v4, v11, vcc
	v_mov_b32_e32 v1, v12
	v_mov_b32_e32 v11, v5
	v_mov_b32_e32 v5, v3

.LBB0_890:
	s_or_b64 exec, exec, s[12:13]
	s_add_i32 s2, s8, 3
	v_readlane_b32 s3, v30, s2
	ds_read_b32 v12, v9 offset:12
	ds_read_b32 v13, v9 offset:4236
	ds_read_b32 v14, v9 offset:8460
	ds_read_b32 v15, v9 offset:12684
	ds_read_b32 v17, v9 offset:16908
	ds_read_b32 v18, v9 offset:21132
	ds_read_b32 v19, v9 offset:25356
	ds_read_b32 v9, v9 offset:29580
	s_waitcnt lgkmcnt(7)
	v_add_f32_e32 v11, s3, v12
	s_waitcnt lgkmcnt(6)
	v_add_f32_e32 v11, v11, v13
	s_waitcnt lgkmcnt(5)
	v_add_f32_e32 v11, v11, v14
	s_waitcnt lgkmcnt(4)
	v_add_f32_e32 v11, v11, v15
	s_waitcnt lgkmcnt(3)
	v_add_f32_e32 v11, v11, v17
	s_waitcnt lgkmcnt(2)
	v_add_f32_e32 v11, v11, v18
	s_waitcnt lgkmcnt(1)
	v_add_f32_e32 v11, v11, v19
	s_waitcnt lgkmcnt(0)
	v_add_f32_e32 v9, v11, v9
	v_cmp_gt_f32_e32 vcc, v9, v10
	s_and_saveexec_b64 s[10:11], vcc
	s_cbranch_execz .LBB0_871
	s_add_i32 s1, s8, 3
	v_cmp_gt_f32_e32 vcc, v9, v6
	v_mov_b32_e32 v3, s1
	s_and_saveexec_b64 s[12:13], vcc
	s_cbranch_execz .LBB0_870
	v_cmp_gt_f32_e32 vcc, v9, v5
	v_mov_b32_e32 v10, s1
	s_and_saveexec_b64 s[14:15], vcc
	s_cbranch_execz .LBB0_869
	v_mov_b32_e32 v3, s1
	v_cmp_gt_f32_e32 vcc, v9, v4
	v_mov_b32_e32 v10, v1
	s_nop 0
	v_cndmask_b32_e32 v11, v3, v0, vcc
	v_cndmask_b32_e32 v0, v0, v3, vcc
	v_cndmask_b32_e32 v3, v9, v4, vcc
	v_cndmask_b32_e32 v4, v4, v9, vcc
	v_mov_b32_e32 v1, v11
	v_mov_b32_e32 v9, v5
	v_mov_b32_e32 v5, v3
	s_branch .LBB0_869
